# conversion groups re-split in sixteenths of the grid (112/48/96 workgroups instead of 128/32/96), halves of a class split by blockIdx bit 7; placement of all later code kept as in v52
# baseline (speedup 1.0000x reference)
.LBB0_202:
	s_bfe_u32 s53, s92, 0x30003
	s_lshr_b32 s46, s92, 7
	s_lshl1_add_u32 s53, s53, s46
	s_cmpk_gt_u32 s92, 0xbf
	s_nop 0
	s_nop 0
	s_nop 0
	s_nop 0
	s_nop 0
	s_nop 0
	s_nop 0
	s_nop 0
	s_nop 0
	s_nop 0
	s_nop 0
	s_nop 0
	s_nop 0
	s_nop 0
	s_cselect_b64 s[0:1], -1, 0
	s_cmpk_eq_i32 s96, 0x100
	s_cselect_b64 s[6:7], -1, 0
	s_and_b64 s[2:3], s[6:7], exec
	s_movk_i32 s2, 0x5800
	v_writelane_b32 v253, s6, 48
	s_cselect_b32 s4, 0x600, 0
	s_cselect_b32 s50, s2, 0x6180
	s_cselect_b32 s95, 0x380, 0
	v_writelane_b32 v253, s7, 49
	s_and_b64 s[6:7], s[0:1], s[6:7]
	s_cmp_gt_u32 s53, 6
	s_mul_i32 s46, s94, s96
	s_cbranch_scc1 .LBB0_563
	s_lshl_b32 s20, s96, 3
	s_abs_i32 s18, s20
	s_waitcnt vmcnt(1)
	v_cvt_f32_u32_e32 v2, s18
	s_sub_i32 s0, 0, s18
	s_add_i32 s14, s20, s50
	s_lshl_b32 s23, s97, 3
	v_rcp_iflag_f32_e32 v2, v2
	s_add_i32 s14, s14, -1
	s_add_i32 s24, s23, s94
	s_abs_i32 s12, s14
	v_mul_f32_e32 v2, 0x4f7ffffe, v2
	v_cvt_u32_f32_e32 v2, v2
	s_nop 0
	v_readfirstlane_b32 s19, v2
	s_mul_i32 s0, s0, s19
	s_mul_hi_u32 s0, s19, s0
	s_add_i32 s19, s19, s0
	s_cmp_ge_i32 s24, s50
	s_mul_hi_u32 s13, s12, s19
	s_cbranch_scc1 .LBB0_211
	s_add_i32 s15, s24, 0xcc0
	s_cmpk_gt_i32 s24, 0xf7ff
	s_cbranch_scc0 .LBB0_212
	s_cmpk_gt_u32 s15, 0x5bf
	s_cbranch_scc0 .LBB0_213
	s_cmpk_gt_u32 s15, 0x6bf
	s_cbranch_scc0 .LBB0_214
	s_cmpk_gt_u32 s15, 0x8bf
	s_cbranch_scc0 .LBB0_215
	s_cmp_lt_u32 s24, 0xfffff340
	s_cbranch_scc0 .LBB0_216
	s_and_b32 s0, s24, 0xffff
	s_mul_i32 s0, s0, 0xaaab
	s_lshr_b32 s10, s0, 24
	s_mul_i32 s11, s10, 0xfffffe80
	s_add_i32 s11, s11, s24
	s_cmpk_gt_i32 s11, 0xff
	s_cbranch_scc0 .LBB0_217
	s_add_i32 s0, s11, 0xffffff00
	s_lshr_b32 s0, s0, 4
	v_readlane_b32 s56, v253, 31
	s_and_b32 s0, s0, 0xffffffe
	s_lshl_b32 s8, s10, 20
	s_lshl_b32 s2, s10, 22
	v_readlane_b32 s66, v253, 41
	v_readlane_b32 s67, v253, 42
	s_add_u32 s2, s66, s2
	s_addc_u32 s3, s67, 0
	s_mov_b32 s1, 0
	s_cmpk_lt_u32 s24, 0x6000
	s_cselect_b32 s9, s3, s85
	s_cselect_b32 s16, s2, s84
	s_lshl_b64 s[2:3], s[0:1], 19
	s_add_u32 s1, s16, s2
	s_addc_u32 s3, s9, s3
	s_lshl_b32 s2, s15, 6
	s_and_b32 s9, s2, 0x7c0
	s_lshl_b32 s2, s9, 2
	s_add_u32 s2, s1, s2
	s_addc_u32 s3, s3, 0
	s_lshl_b32 s1, s9, 9
	s_add_u32 s8, s90, s8
	s_addc_u32 s9, s91, 0
	s_add_u32 s1, s8, s1
	s_addc_u32 s8, s9, 0
	s_lshl_b32 s0, s0, 6
	s_add_u32 s0, s1, s0
	s_addc_u32 s1, s8, 0
	s_add_u32 s0, s0, 0x30c00000
	v_readlane_b32 s57, v253, 32
	v_readlane_b32 s58, v253, 33
	v_readlane_b32 s59, v253, 34
	v_readlane_b32 s60, v253, 35
	v_readlane_b32 s61, v253, 36
	v_readlane_b32 s62, v253, 37
	v_readlane_b32 s63, v253, 38
	v_readlane_b32 s64, v253, 39
	v_readlane_b32 s65, v253, 40
	v_readlane_b32 s68, v253, 43
	v_readlane_b32 s69, v253, 44
	v_readlane_b32 s70, v253, 45
	v_readlane_b32 s71, v253, 46
	s_addc_u32 s1, s1, 0
	s_mov_b64 s[8:9], 0
	s_branch .LBB0_218

.LBB0_699:
	s_cmp_ge_u32 s53, 7
	s_cselect_b32 s36, 1, 0
	s_cmp_ge_u32 s53, 10
	s_cselect_b32 s53, 1, 0
	s_add_i32 s36, s36, s53
	v_readlane_b32 s84, v253, 22
	s_cmp_lg_u32 s36, 1
	v_readlane_b32 s85, v253, 23
	v_readlane_b32 s86, v253, 24
	v_readlane_b32 s87, v253, 25
	v_readlane_b32 s88, v253, 26
	v_readlane_b32 s89, v253, 27
	v_readlane_b32 s90, v253, 28
	v_readlane_b32 s91, v253, 29
	s_cbranch_scc1 .LBB0_1060
	s_lshl_b32 s22, s96, 3
	s_abs_i32 s20, s22
	v_cvt_f32_u32_e32 v2, s20
	s_sub_i32 s0, 0, s20
	s_add_i32 s16, s22, s50
	s_lshl_b32 s25, s97, 3
	v_rcp_iflag_f32_e32 v2, v2
	s_add_i32 s16, s16, -1
	s_add_i32 s26, s25, s94
	s_abs_i32 s14, s16
	v_mul_f32_e32 v2, 0x4f7ffffe, v2
	v_cvt_u32_f32_e32 v2, v2
	s_waitcnt vmcnt(0) lgkmcnt(0)
	s_barrier
	v_readfirstlane_b32 s21, v2
	s_mul_i32 s0, s0, s21
	s_mul_hi_u32 s0, s21, s0
	s_add_i32 s21, s21, s0
	s_cmp_ge_i32 s26, s50
	s_mul_hi_u32 s15, s14, s21
	s_cbranch_scc1 .LBB0_708
	s_add_i32 s17, s26, 0xcc0
	s_cmpk_gt_i32 s26, 0xf7ff
	s_cbranch_scc0 .LBB0_709
	s_cmpk_gt_u32 s17, 0x5bf
	s_cbranch_scc0 .LBB0_710
	s_cmpk_gt_u32 s17, 0x6bf
	s_cbranch_scc0 .LBB0_711
	s_cmpk_gt_u32 s17, 0x8bf
	s_cbranch_scc0 .LBB0_712
	s_cmp_lt_u32 s26, 0xfffff340
	s_cbranch_scc0 .LBB0_713
	s_mul_hi_u32 s0, s26, 0xaaaaaaab
	s_lshr_b32 s10, s0, 8
	s_mul_i32 s18, s10, 0xfffffe80
	s_add_i32 s18, s18, s26
	s_cmpk_gt_i32 s18, 0xff
	s_cbranch_scc0 .LBB0_714
	s_add_i32 s0, s18, 0xffffff00
	s_lshr_b32 s0, s0, 4
	s_lshl_b32 s12, s10, 20
	s_mov_b32 s13, 0
	v_readlane_b32 s56, v253, 31
	s_and_b32 s0, s0, 0xffffffe
	s_lshl_b64 s[2:3], s[12:13], 2
	v_readlane_b32 s66, v253, 41
	v_readlane_b32 s67, v253, 42
	s_add_u32 s1, s66, s2
	s_addc_u32 s2, s67, s3
	s_cmpk_lt_u32 s26, 0x6000
	s_cselect_b32 s12, s1, s84
	s_mov_b32 s1, s13
	s_cselect_b32 s11, s2, s85
	s_lshl_b64 s[2:3], s[0:1], 19
	s_add_u32 s1, s12, s2
	s_addc_u32 s3, s11, s3
	s_lshl_b32 s2, s26, 6
	s_and_b32 s19, s2, 0x7c0
	s_lshl_b32 s2, s19, 2
	s_add_u32 s2, s1, s2
	s_mov_b32 s11, s13
	s_addc_u32 s3, s3, 0
	s_lshl_b64 s[12:13], s[10:11], 20
	s_lshl_b32 s1, s19, 9
	s_add_u32 s11, s90, s12
	s_addc_u32 s12, s91, s13
	s_add_u32 s1, s11, s1
	s_addc_u32 s11, s12, 0
	s_lshl_b32 s0, s0, 6
	s_add_u32 s0, s1, s0
	s_addc_u32 s1, s11, 0
	s_add_u32 s0, s0, 0x30c00000
	v_readlane_b32 s57, v253, 32
	v_readlane_b32 s58, v253, 33
	v_readlane_b32 s59, v253, 34
	v_readlane_b32 s60, v253, 35
	v_readlane_b32 s61, v253, 36
	v_readlane_b32 s62, v253, 37
	v_readlane_b32 s63, v253, 38
	v_readlane_b32 s64, v253, 39
	v_readlane_b32 s65, v253, 40
	v_readlane_b32 s68, v253, 43
	v_readlane_b32 s69, v253, 44
	v_readlane_b32 s70, v253, 45
	v_readlane_b32 s71, v253, 46
	s_addc_u32 s1, s1, 0
	s_mov_b64 s[12:13], 0
	s_branch .LBB0_715
